# speedup vs baseline: 1.0216x; 1.0216x over previous
_Z10rnn_kernelPKDF16_S0_PDF16_S1_:
	s_load_dwordx8 s[4:11], s[0:1], 0x0
	v_readfirstlane_b32 s0, v0
	s_lshr_b32 s12, s0, 6
	s_lshl_b32 s0, s12, 4
	s_mov_b32 s1, 0
	s_lshl_b64 s[14:15], s[0:1], 13
	v_and_b32_e32 v1, 63, v0
	s_waitcnt lgkmcnt(0)
	s_add_u32 s6, s6, s14
	s_addc_u32 s7, s7, s15
	v_lshlrev_b32_e32 v142, 4, v1
	v_mov_b32_e32 v143, 0
	v_lshl_add_u64 v[2:3], s[6:7], 0, v[142:143]
	s_movk_i32 s3, 0x1000
	v_add_co_u32_e32 v4, vcc, s3, v2
	s_mov_b32 s13, 0x18000
	s_nop 0
	v_addc_co_u32_e32 v5, vcc, 0, v3, vcc
	v_add_co_u32_e32 v110, vcc, s13, v2
	s_mov_b32 s13, 0x19000
	s_nop 0
	v_addc_co_u32_e32 v111, vcc, 0, v3, vcc
	v_add_co_u32_e32 v50, vcc, s13, v2
	s_mov_b32 s13, 0x1a000
	s_nop 0
	v_addc_co_u32_e32 v51, vcc, 0, v3, vcc
	v_add_co_u32_e32 v52, vcc, s13, v2
	s_movk_i32 s3, 0x2000
	s_nop 0
	v_addc_co_u32_e32 v53, vcc, 0, v3, vcc
	v_add_co_u32_e32 v54, vcc, s3, v2
	s_movk_i32 s3, 0x3000
	s_nop 0
	v_addc_co_u32_e32 v55, vcc, 0, v3, vcc
	global_load_dwordx4 v[6:9], v[110:111], off
	global_load_dwordx4 v[10:13], v[110:111], off offset:1024
	global_load_dwordx4 v[14:17], v[110:111], off offset:2048
	global_load_dwordx4 v[18:21], v[110:111], off offset:3072
	global_load_dwordx4 v[22:25], v[50:51], off offset:1024
	global_load_dwordx4 v[26:29], v[50:51], off offset:2048
	global_load_dwordx4 a[0:3], v[4:5], off offset:1024
	global_load_dwordx4 a[4:7], v[4:5], off offset:2048
	global_load_dwordx4 a[8:11], v[54:55], off offset:-4096
	global_load_dwordx4 a[12:15], v[54:55], off
	global_load_dwordx4 a[16:19], v[54:55], off offset:1024
	global_load_dwordx4 a[20:23], v[54:55], off offset:2048
	global_load_dwordx4 v[30:33], v[50:51], off offset:3072
	global_load_dwordx4 v[34:37], v[52:53], off offset:-4096
	global_load_dwordx4 v[38:41], v[52:53], off
	global_load_dwordx4 v[42:45], v[52:53], off offset:1024
	global_load_dwordx4 v[46:49], v[52:53], off offset:2048
	v_add_co_u32_e32 v50, vcc, s3, v2
	s_movk_i32 s3, 0x4000
	s_nop 0
	v_addc_co_u32_e32 v51, vcc, 0, v3, vcc
	v_add_co_u32_e32 v56, vcc, s3, v2
	s_movk_i32 s3, 0x5000
	s_nop 0
	v_addc_co_u32_e32 v57, vcc, 0, v3, vcc
	global_load_dwordx4 a[24:27], v[54:55], off offset:3072
	global_load_dwordx4 a[28:31], v[56:57], off offset:-4096
	global_load_dwordx4 a[32:35], v[4:5], off offset:3072
	global_load_dwordx4 a[36:39], v[50:51], off offset:1024
	global_load_dwordx4 a[40:43], v[50:51], off offset:2048
	global_load_dwordx4 a[44:47], v[50:51], off offset:3072
	global_load_dwordx4 a[48:51], v[56:57], off
	global_load_dwordx4 a[52:55], v[56:57], off offset:1024
	global_load_dwordx4 a[56:59], v[56:57], off offset:2048
	global_load_dwordx4 a[60:63], v[56:57], off offset:3072
	v_add_co_u32_e32 v4, vcc, s3, v2
	s_movk_i32 s3, 0x6000
	s_nop 0
	v_addc_co_u32_e32 v5, vcc, 0, v3, vcc
	v_add_co_u32_e32 v98, vcc, s3, v2
	s_movk_i32 s3, 0x7000
	s_nop 0
	v_addc_co_u32_e32 v99, vcc, 0, v3, vcc
	v_add_co_u32_e32 v100, vcc, s3, v2
	s_mov_b32 s3, 0x8000
	s_nop 0
	v_addc_co_u32_e32 v101, vcc, 0, v3, vcc
	global_load_dwordx4 v[50:53], v[52:53], off offset:3072
	v_add_co_u32_e32 v102, vcc, s3, v2
	s_mov_b32 s14, 0x1c000
	s_nop 0
	v_addc_co_u32_e32 v103, vcc, 0, v3, vcc
	v_add_co_u32_e32 v82, vcc, s14, v2
	global_load_dwordx4 a[64:67], v[4:5], off offset:1024
	global_load_dwordx4 a[68:71], v[4:5], off offset:2048
	global_load_dwordx4 a[72:75], v[98:99], off offset:-4096
	global_load_dwordx4 a[76:79], v[98:99], off
	global_load_dwordx4 a[80:83], v[98:99], off offset:1024
	global_load_dwordx4 a[84:87], v[98:99], off offset:2048
	v_addc_co_u32_e32 v83, vcc, 0, v3, vcc
	global_load_dwordx4 v[54:57], v[82:83], off offset:-4096
	s_mov_b32 s13, 0x1b000
	v_add_co_u32_e32 v66, vcc, s13, v2
	s_mov_b32 s13, 0x1d000
	s_nop 0
	v_addc_co_u32_e32 v67, vcc, 0, v3, vcc
	global_load_dwordx4 v[58:61], v[66:67], off offset:1024
	global_load_dwordx4 v[62:65], v[66:67], off offset:2048
	s_nop 0
	global_load_dwordx4 v[66:69], v[66:67], off offset:3072
	s_nop 0
	global_load_dwordx4 v[70:73], v[82:83], off
	global_load_dwordx4 v[74:77], v[82:83], off offset:1024
	global_load_dwordx4 v[78:81], v[82:83], off offset:2048
	s_nop 0
	global_load_dwordx4 v[82:85], v[82:83], off offset:3072
	v_add_co_u32_e32 v104, vcc, s13, v2
	s_mov_b32 s13, 0x1e000
	s_nop 0
	v_addc_co_u32_e32 v105, vcc, 0, v3, vcc
	v_add_co_u32_e32 v106, vcc, s13, v2
	s_lshl_b32 s13, s12, 15
	s_nop 0
	v_addc_co_u32_e32 v107, vcc, 0, v3, vcc
	global_load_dwordx4 v[86:89], v[106:107], off offset:-4096
	global_load_dwordx4 v[90:93], v[104:105], off offset:1024
	global_load_dwordx4 v[94:97], v[104:105], off offset:2048
	global_load_dwordx4 a[88:91], v[98:99], off offset:3072
	global_load_dwordx4 a[92:95], v[102:103], off offset:-4096
	global_load_dwordx4 a[96:99], v[4:5], off offset:3072
	global_load_dwordx4 a[100:103], v[100:101], off offset:1024
	global_load_dwordx4 a[104:107], v[100:101], off offset:2048
	global_load_dwordx4 a[108:111], v[100:101], off offset:3072
	global_load_dwordx4 a[112:115], v[102:103], off
	global_load_dwordx4 a[116:119], v[102:103], off offset:1024
	global_load_dwordx4 a[120:123], v[102:103], off offset:2048
	global_load_dwordx4 a[124:127], v[102:103], off offset:3072
	s_add_i32 s13, s13, 0
	v_add_u32_e32 v213, s13, v142
	s_mov_b32 s13, 0x9000
	s_waitcnt vmcnt(54)
	ds_write_b128 v213, v[6:9]
	s_waitcnt vmcnt(53)
	ds_write_b128 v213, v[10:13] offset:1024
	s_waitcnt vmcnt(52)
	ds_write_b128 v213, v[14:17] offset:2048
	s_waitcnt vmcnt(51)
	ds_write_b128 v213, v[18:21] offset:3072
	s_waitcnt vmcnt(41)
	ds_write_b128 v213, v[34:37] offset:4096
	ds_write_b128 v213, v[22:25] offset:5120
	ds_write_b128 v213, v[26:29] offset:6144
	ds_write_b128 v213, v[30:33] offset:7168
	s_waitcnt vmcnt(40)
	ds_write_b128 v213, v[38:41] offset:8192
	s_waitcnt vmcnt(39)
	ds_write_b128 v213, v[42:45] offset:9216
	s_waitcnt vmcnt(38)
	ds_write_b128 v213, v[46:49] offset:10240
	v_add_co_u32_e32 v8, vcc, s13, v2
	s_mov_b32 s13, 0xa000
	s_nop 0
	v_addc_co_u32_e32 v9, vcc, 0, v3, vcc
	v_add_co_u32_e32 v10, vcc, s13, v2
	s_mov_b32 s13, 0xb000
	s_nop 0
	v_addc_co_u32_e32 v11, vcc, 0, v3, vcc
	v_add_co_u32_e32 v12, vcc, s13, v2
	s_mov_b32 s13, 0xc000
	s_nop 0
	v_addc_co_u32_e32 v13, vcc, 0, v3, vcc
	v_and_b32_e32 v32, 15, v0
	v_lshl_or_b32 v206, s2, 4, v32
	v_ashrrev_i32_e32 v207, 31, v206
	v_bfe_u32 v1, v0, 5, 1
	v_lshlrev_b64 v[144:145], 10, v[206:207]
	v_or_b32_e32 v33, s0, v1
	v_bitop3_b32 v1, v1, v32, s0 bitop3:0x36
	s_lshl_b32 s0, s12, 8
	s_mov_b32 s2, 0x400000
	v_bitop3_b32 v153, v33, v32, 12 bitop3:0x36
	v_bitop3_b32 v154, v33, v32, 14 bitop3:0x36
	s_waitcnt vmcnt(27)
	ds_write_b128 v213, v[50:53] offset:11264
	global_load_dwordx4 a[128:131], v[8:9], off offset:1024
	global_load_dwordx4 a[132:135], v[8:9], off offset:2048
	global_load_dwordx4 a[136:139], v[10:11], off offset:-4096
	global_load_dwordx4 a[140:143], v[10:11], off
	global_load_dwordx4 v[4:7], v[104:105], off offset:3072
	global_load_dwordx4 a[144:147], v[10:11], off offset:1024
	global_load_dwordx4 a[148:151], v[10:11], off offset:2048
	global_load_dwordx4 a[152:155], v[8:9], off offset:3072
	global_load_dwordx4 a[156:159], v[12:13], off offset:1024
	global_load_dwordx4 a[160:163], v[12:13], off offset:2048
	global_load_dwordx4 a[164:167], v[12:13], off offset:3072
	v_add_co_u32_e32 v12, vcc, s13, v2
	v_bfe_u32 v218, v0, 4, 2
	s_nop 0
	v_addc_co_u32_e32 v13, vcc, 0, v3, vcc
	global_load_dwordx4 a[168:171], v[10:11], off offset:3072
	global_load_dwordx4 a[172:175], v[12:13], off offset:-4096
	s_waitcnt vmcnt(33)
	ds_write_b128 v213, v[54:57] offset:12288
	global_load_dwordx4 v[8:11], v[106:107], off
	global_load_dwordx4 a[176:179], v[12:13], off
	global_load_dwordx4 a[180:183], v[12:13], off offset:1024
	global_load_dwordx4 a[184:187], v[12:13], off offset:2048
	global_load_dwordx4 a[188:191], v[12:13], off offset:3072
	s_waitcnt vmcnt(37)
	ds_write_b128 v213, v[58:61] offset:13312
	global_load_dwordx4 v[12:15], v[106:107], off offset:1024
	global_load_dwordx4 a[192:195], v142, s[6:7]
	global_load_dwordx4 a[196:199], v142, s[6:7] offset:1024
	global_load_dwordx4 a[200:203], v142, s[6:7] offset:2048
	global_load_dwordx4 a[204:207], v142, s[6:7] offset:3072
	s_mov_b32 s7, 0x1f000
	v_add_co_u32_e32 v16, vcc, s7, v2
	s_waitcnt vmcnt(41)
	ds_write_b128 v213, v[62:65] offset:14336
	global_load_dwordx4 v[24:27], v[106:107], off offset:2048
	s_waitcnt vmcnt(41)
	ds_write_b128 v213, v[66:69] offset:15360
	s_waitcnt vmcnt(40)
	ds_write_b128 v213, v[70:73] offset:16384
	s_waitcnt vmcnt(39)
	ds_write_b128 v213, v[74:77] offset:17408
	s_waitcnt vmcnt(38)
	ds_write_b128 v213, v[78:81] offset:18432
	s_waitcnt vmcnt(37)
	ds_write_b128 v213, v[82:85] offset:19456
	s_waitcnt vmcnt(36)
	ds_write_b128 v213, v[86:89] offset:20480
	s_waitcnt vmcnt(35)
	ds_write_b128 v213, v[90:93] offset:21504
	s_waitcnt vmcnt(34)
	ds_write_b128 v213, v[94:97] offset:22528
	v_addc_co_u32_e32 v17, vcc, 0, v3, vcc
	global_load_dwordx4 v[28:31], v[106:107], off offset:3072
	global_load_dwordx4 v[36:39], v[16:17], off
	global_load_dwordx4 v[40:43], v[16:17], off offset:1024
	global_load_dwordx4 v[48:51], v[16:17], off offset:2048
	global_load_dwordx4 v[52:55], v[16:17], off offset:3072
	v_lshl_add_u64 v[16:17], s[4:5], 0, v[144:145]
	v_lshl_add_u64 v[16:17], v[16:17], 0, s[0:1]
	v_and_b32_e32 v142, 48, v0
	v_lshl_add_u64 v[18:19], v[16:17], 0, v[142:143]
	global_load_dwordx4 v[56:59], v[18:19], off
	s_mov_b32 s1, 0xe000
	v_add_co_u32_e32 v16, vcc, s1, v2
	s_mov_b32 s6, 0xd000
	s_nop 0
	v_addc_co_u32_e32 v17, vcc, 0, v3, vcc
	v_add_co_u32_e32 v20, vcc, s6, v2
	s_mov_b32 s1, 0xf000
	s_nop 0
	v_addc_co_u32_e32 v21, vcc, 0, v3, vcc
	global_load_dwordx4 a[208:211], v[16:17], off offset:-4096
	global_load_dwordx4 a[212:215], v[16:17], off
	global_load_dwordx4 a[216:219], v[16:17], off offset:1024
	global_load_dwordx4 a[220:223], v[16:17], off offset:2048
	global_load_dwordx4 a[224:227], v[20:21], off offset:1024
	global_load_dwordx4 a[228:231], v[20:21], off offset:2048
	v_lshlrev_b32_e32 v143, 10, v32
	v_or_b32_e32 v144, v144, v142
	s_waitcnt vmcnt(31)
	ds_write_b128 v213, v[4:7] offset:23552
	v_add_co_u32_e32 v6, vcc, s1, v2
	s_mov_b32 s1, 0x10000
	s_nop 0
	v_addc_co_u32_e32 v7, vcc, 0, v3, vcc
	v_add_co_u32_e32 v22, vcc, s1, v2
	s_mov_b32 s1, 0x11000
	s_nop 0
	v_addc_co_u32_e32 v23, vcc, 0, v3, vcc
	global_load_dwordx4 a[232:235], v[16:17], off offset:3072
	global_load_dwordx4 a[236:239], v[22:23], off offset:-4096
	global_load_dwordx4 a[240:243], v[20:21], off offset:3072
	global_load_dwordx4 a[244:247], v[6:7], off offset:1024
	s_waitcnt vmcnt(26)
	ds_write_b128 v213, v[8:11] offset:24576
	s_waitcnt vmcnt(21)
	ds_write_b128 v213, v[12:15] offset:25600
	global_load_dwordx4 v[10:13], v[18:19], off offset:64
	v_add_co_u32_e32 v34, vcc, s1, v2
	s_mov_b32 s1, 0x12000
	s_nop 0
	v_addc_co_u32_e32 v35, vcc, 0, v3, vcc
	v_add_co_u32_e32 v66, vcc, s1, v2
	s_mov_b32 s1, 0x13000
	s_nop 0
	v_addc_co_u32_e32 v67, vcc, 0, v3, vcc
	v_add_co_u32_e32 v46, vcc, s1, v2
	s_mov_b32 s1, 0x14000
	s_nop 0
	v_addc_co_u32_e32 v47, vcc, 0, v3, vcc
	v_add_co_u32_e32 v86, vcc, s1, v2
	s_mov_b32 s1, 0x15000
	s_nop 0
	v_addc_co_u32_e32 v87, vcc, 0, v3, vcc
	v_add_co_u32_e32 v122, vcc, s1, v2
	s_mov_b32 s1, 0x16000
	s_nop 0
	v_addc_co_u32_e32 v123, vcc, 0, v3, vcc
	v_lshrrev_b32_e32 v14, 1, v0
	v_add_co_u32_e32 v106, vcc, s1, v2
	v_and_or_b32 v152, v14, 8, v143
	s_waitcnt vmcnt(11)
	v_cvt_f32_f16_e32 v14, v56
	v_addc_co_u32_e32 v107, vcc, 0, v3, vcc
	s_mov_b32 s1, 0x17000
	ds_write_b128 v213, v[24:27] offset:26624
	ds_write_b128 v213, v[28:31] offset:27648
	v_add_co_u32_e32 v134, vcc, s1, v2
	ds_write_b128 v213, v[36:39] offset:28672
	s_nop 0
	v_addc_co_u32_e32 v135, vcc, 0, v3, vcc
	global_load_dwordx4 v[2:5], v[6:7], off offset:2048
	s_nop 0
	global_load_dwordx4 v[6:9], v[6:7], off offset:3072
	ds_write_b128 v213, v[40:43] offset:29696
	ds_write_b128 v213, v[48:51] offset:30720
	ds_write_b128 v213, v[52:55] offset:31744
	v_lshl_add_u32 v217, v1, 4, v152
	v_bitop3_b32 v1, v33, v32, 2 bitop3:0x36
	v_lshl_add_u32 v215, v1, 4, v152
	v_exp_f32_e32 v1, v14
	global_load_dwordx4 v[14:17], v[18:19], off offset:128
	global_load_dwordx4 v[138:141], v[18:19], off offset:192
	v_cvt_f32_f16_sdwa v20, v56 dst_sel:DWORD dst_unused:UNUSED_PAD src0_sel:WORD_1
	v_cvt_f32_f16_e32 v21, v57
	v_cvt_f32_f16_sdwa v25, v57 dst_sel:DWORD dst_unused:UNUSED_PAD src0_sel:WORD_1
	v_add_f32_e32 v1, 1.0, v1
	v_exp_f32_e32 v24, v20
	v_rcp_f32_e32 v20, v1
	v_exp_f32_e32 v1, v21
	v_exp_f32_e32 v25, v25
	v_add_f32_e32 v21, 1.0, v24
	v_rcp_f32_e32 v21, v21
	v_add_f32_e32 v1, 1.0, v1
	v_rcp_f32_e32 v24, v1
	v_add_f32_e32 v1, 1.0, v25
	v_rcp_f32_e32 v25, v1
	v_pk_fma_f32 v[20:21], v[20:21], 2.0, 1.0 op_sel_hi:[1,0,0] neg_lo:[1,0,0] neg_hi:[1,0,0]
	v_cvt_f32_f16_e32 v1, v58
	s_add_i32 s1, 0, 0x24000
	v_pk_fma_f32 v[24:25], v[24:25], 2.0, 1.0 op_sel_hi:[1,0,0] neg_lo:[1,0,0] neg_hi:[1,0,0]
	v_cvt_pk_f16_f32 v20, v20, v21
	v_cvt_pk_f16_f32 v21, v24, v25
	v_add_u32_e32 v24, s1, v217
	ds_write_b64 v24, v[20:21]
	v_cvt_f32_f16_sdwa v20, v58 dst_sel:DWORD dst_unused:UNUSED_PAD src0_sel:WORD_1
	v_exp_f32_e32 v1, v1
	v_cvt_f32_f16_e32 v21, v59
	v_cvt_f32_f16_sdwa v24, v59 dst_sel:DWORD dst_unused:UNUSED_PAD src0_sel:WORD_1
	v_exp_f32_e32 v25, v20
	v_add_f32_e32 v1, 1.0, v1
	v_rcp_f32_e32 v20, v1
	v_exp_f32_e32 v1, v21
	v_add_f32_e32 v21, 1.0, v25
	v_exp_f32_e32 v25, v24
	v_rcp_f32_e32 v21, v21
	v_add_f32_e32 v1, 1.0, v1
	v_rcp_f32_e32 v24, v1
	v_add_f32_e32 v1, 1.0, v25
	v_rcp_f32_e32 v25, v1
	s_waitcnt vmcnt(4)
	v_cvt_f32_f16_e32 v1, v10
	v_cvt_f32_f16_sdwa v10, v10 dst_sel:DWORD dst_unused:UNUSED_PAD src0_sel:WORD_1
	v_pk_fma_f32 v[20:21], v[20:21], 2.0, 1.0 op_sel_hi:[1,0,0] neg_lo:[1,0,0] neg_hi:[1,0,0]
	v_pk_fma_f32 v[24:25], v[24:25], 2.0, 1.0 op_sel_hi:[1,0,0] neg_lo:[1,0,0] neg_hi:[1,0,0]
	v_cvt_pk_f16_f32 v20, v20, v21
	v_cvt_pk_f16_f32 v21, v24, v25
	v_exp_f32_e32 v1, v1
	v_add_u32_e32 v24, s1, v215
	ds_write_b64 v24, v[20:21]
	v_cvt_f32_f16_e32 v20, v11
	v_exp_f32_e32 v21, v10
	v_cvt_f32_f16_sdwa v11, v11 dst_sel:DWORD dst_unused:UNUSED_PAD src0_sel:WORD_1
	v_add_f32_e32 v1, 1.0, v1
	v_rcp_f32_e32 v10, v1
	v_exp_f32_e32 v1, v20
	v_add_f32_e32 v20, 1.0, v21
	v_exp_f32_e32 v21, v11
	v_rcp_f32_e32 v11, v20
	v_add_f32_e32 v1, 1.0, v1
	v_rcp_f32_e32 v20, v1
	v_add_f32_e32 v1, 1.0, v21
	v_rcp_f32_e32 v21, v1
	v_bitop3_b32 v26, v33, v32, 4 bitop3:0x36
	v_bitop3_b32 v1, v33, v32, 6 bitop3:0x36
	v_lshl_add_u32 v211, v26, 4, v152
	v_lshl_add_u32 v212, v1, 4, v152
	v_pk_fma_f32 v[10:11], v[10:11], 2.0, 1.0 op_sel_hi:[1,0,0] neg_lo:[1,0,0] neg_hi:[1,0,0]
	v_pk_fma_f32 v[20:21], v[20:21], 2.0, 1.0 op_sel_hi:[1,0,0] neg_lo:[1,0,0] neg_hi:[1,0,0]
	v_bitop3_b32 v1, v33, v32, 8 bitop3:0x36
	v_cvt_pk_f16_f32 v10, v10, v11
	v_cvt_pk_f16_f32 v11, v20, v21
	v_lshl_add_u32 v210, v1, 4, v152
	v_add_u32_e32 v1, s1, v211
	ds_write_b64 v1, v[10:11]
	v_cvt_f32_f16_e32 v10, v12
	v_cvt_f32_f16_sdwa v11, v12 dst_sel:DWORD dst_unused:UNUSED_PAD src0_sel:WORD_1
	v_cvt_f32_f16_e32 v12, v13
	v_cvt_f32_f16_sdwa v13, v13 dst_sel:DWORD dst_unused:UNUSED_PAD src0_sel:WORD_1
	v_exp_f32_e32 v10, v10
	v_exp_f32_e32 v11, v11
	v_exp_f32_e32 v12, v12
	v_exp_f32_e32 v13, v13
	v_add_f32_e32 v10, 1.0, v10
	v_add_f32_e32 v11, 1.0, v11
	v_add_f32_e32 v12, 1.0, v12
	v_add_f32_e32 v13, 1.0, v13
	v_rcp_f32_e32 v10, v10
	v_rcp_f32_e32 v11, v11
	v_rcp_f32_e32 v12, v12
	v_rcp_f32_e32 v13, v13
	s_waitcnt vmcnt(1)
	v_cvt_f32_f16_e32 v20, v14
	v_pk_fma_f32 v[10:11], v[10:11], 2.0, 1.0 op_sel_hi:[1,0,0] neg_lo:[1,0,0] neg_hi:[1,0,0]
	v_cvt_f32_f16_sdwa v14, v14 dst_sel:DWORD dst_unused:UNUSED_PAD src0_sel:WORD_1
	v_pk_fma_f32 v[12:13], v[12:13], 2.0, 1.0 op_sel_hi:[1,0,0] neg_lo:[1,0,0] neg_hi:[1,0,0]
	v_cvt_pk_f16_f32 v10, v10, v11
	v_cvt_pk_f16_f32 v11, v12, v13
	v_add_u32_e32 v13, s1, v212
	v_exp_f32_e32 v12, v20
	ds_write_b64 v13, v[10:11]
	v_cvt_f32_f16_e32 v11, v15
	v_cvt_f32_f16_sdwa v13, v15 dst_sel:DWORD dst_unused:UNUSED_PAD src0_sel:WORD_1
	v_add_f32_e32 v10, 1.0, v12
	v_exp_f32_e32 v12, v14
	v_exp_f32_e32 v14, v11
	v_exp_f32_e32 v13, v13
	v_rcp_f32_e32 v10, v10
	v_add_f32_e32 v11, 1.0, v12
	v_add_f32_e32 v12, 1.0, v14
	v_add_f32_e32 v13, 1.0, v13
	v_rcp_f32_e32 v11, v11
	v_rcp_f32_e32 v12, v12
	v_rcp_f32_e32 v13, v13
	v_cvt_f32_f16_e32 v14, v16
	v_pk_fma_f32 v[10:11], v[10:11], 2.0, 1.0 op_sel_hi:[1,0,0] neg_lo:[1,0,0] neg_hi:[1,0,0]
	v_add_co_u32_e32 v150, vcc, s2, v18
	v_pk_fma_f32 v[12:13], v[12:13], 2.0, 1.0 op_sel_hi:[1,0,0] neg_lo:[1,0,0] neg_hi:[1,0,0]
	v_cvt_pk_f16_f32 v10, v10, v11
	v_cvt_pk_f16_f32 v11, v12, v13
	v_exp_f32_e32 v12, v14
	v_cvt_f32_f16_sdwa v14, v16 dst_sel:DWORD dst_unused:UNUSED_PAD src0_sel:WORD_1
	v_add_u32_e32 v13, s1, v210
	ds_write_b64 v13, v[10:11]
	v_add_f32_e32 v10, 1.0, v12
	v_cvt_f32_f16_e32 v11, v17
	v_exp_f32_e32 v12, v14
	v_cvt_f32_f16_sdwa v13, v17 dst_sel:DWORD dst_unused:UNUSED_PAD src0_sel:WORD_1
	v_rcp_f32_e32 v10, v10
	v_exp_f32_e32 v14, v11
	v_add_f32_e32 v11, 1.0, v12
	v_exp_f32_e32 v12, v13
	v_rcp_f32_e32 v11, v11
	v_add_f32_e32 v13, 1.0, v14
	v_bitop3_b32 v1, v33, v32, 10 bitop3:0x36
	v_add_f32_e32 v12, 1.0, v12
	v_rcp_f32_e32 v146, v13
	v_rcp_f32_e32 v147, v12
	v_pk_fma_f32 v[148:149], v[10:11], 2.0, 1.0 op_sel_hi:[1,0,0] neg_lo:[1,0,0] neg_hi:[1,0,0]
	global_load_dwordx4 v[10:13], v[22:23], off
	global_load_dwordx4 v[14:17], v[22:23], off offset:1024
	v_addc_co_u32_e32 v151, vcc, 0, v19, vcc
	global_load_dwordx4 v[18:21], v[22:23], off offset:2048
	s_nop 0
	global_load_dwordx4 v[22:25], v[22:23], off offset:3072
	s_nop 0
	global_load_dwordx4 v[26:29], v[34:35], off offset:1024
	global_load_dwordx4 v[30:33], v[34:35], off offset:2048
	s_nop 0
	global_load_dwordx4 v[34:37], v[34:35], off offset:3072
	s_nop 0
	global_load_dwordx4 v[38:41], v[46:47], off offset:1024
	global_load_dwordx4 v[42:45], v[46:47], off offset:2048
	s_nop 0
	global_load_dwordx4 v[46:49], v[46:47], off offset:3072
	s_nop 0
	global_load_dwordx4 v[50:53], v[66:67], off offset:-4096
	global_load_dwordx4 v[54:57], v[66:67], off
	global_load_dwordx4 v[58:61], v[66:67], off offset:1024
	global_load_dwordx4 v[62:65], v[66:67], off offset:2048
	s_nop 0
	global_load_dwordx4 v[66:69], v[66:67], off offset:3072
	s_nop 0
	global_load_dwordx4 v[70:73], v[86:87], off offset:-4096
	global_load_dwordx4 v[74:77], v[86:87], off
	global_load_dwordx4 v[78:81], v[86:87], off offset:1024
	global_load_dwordx4 v[82:85], v[86:87], off offset:2048
	s_nop 0
	global_load_dwordx4 v[86:89], v[86:87], off offset:3072
	s_nop 0
	global_load_dwordx4 v[90:93], v[106:107], off offset:-4096
	global_load_dwordx4 v[94:97], v[106:107], off
	global_load_dwordx4 v[98:101], v[106:107], off offset:1024
	global_load_dwordx4 v[102:105], v[106:107], off offset:2048
	s_nop 0
	global_load_dwordx4 v[106:109], v[106:107], off offset:3072
	s_nop 0
	global_load_dwordx4 v[110:113], v[110:111], off offset:-4096
	s_nop 0
	global_load_dwordx4 v[114:117], v[122:123], off offset:1024
	global_load_dwordx4 v[118:121], v[122:123], off offset:2048
	s_nop 0
	global_load_dwordx4 v[122:125], v[122:123], off offset:3072
	s_nop 0
	global_load_dwordx4 v[126:129], v[134:135], off offset:1024
	global_load_dwordx4 v[130:133], v[134:135], off offset:2048
	s_nop 0
	global_load_dwordx4 v[134:137], v[134:135], off offset:3072
	s_nop 0
	global_load_dwordx4 v[178:181], v[150:151], off
	global_load_dwordx4 v[174:177], v[150:151], off offset:64
	global_load_dwordx4 v[170:173], v[150:151], off offset:128
	global_load_dwordx4 v[202:205], v[150:151], off offset:192
	s_waitcnt vmcnt(36)
	v_cvt_f32_f16_e32 v155, v138
	v_cvt_f32_f16_sdwa v138, v138 dst_sel:DWORD dst_unused:UNUSED_PAD src0_sel:WORD_1
	v_pk_fma_f32 v[146:147], v[146:147], 2.0, 1.0 op_sel_hi:[1,0,0] neg_lo:[1,0,0] neg_hi:[1,0,0]
	v_cvt_pk_f16_f32 v148, v148, v149
	v_exp_f32_e32 v150, v155
	v_cvt_pk_f16_f32 v149, v146, v147
	v_cvt_f32_f16_e32 v147, v139
	v_cvt_f32_f16_sdwa v139, v139 dst_sel:DWORD dst_unused:UNUSED_PAD src0_sel:WORD_1
	v_add_f32_e32 v146, 1.0, v150
	v_exp_f32_e32 v150, v138
	v_rcp_f32_e32 v138, v146
	v_exp_f32_e32 v146, v147
	v_lshl_add_u32 v1, v1, 4, v152
	v_add_f32_e32 v147, 1.0, v150
	v_exp_f32_e32 v150, v139
	v_rcp_f32_e32 v139, v147
	v_add_f32_e32 v146, 1.0, v146
	v_rcp_f32_e32 v146, v146
	v_add_f32_e32 v147, 1.0, v150
	v_rcp_f32_e32 v147, v147
	v_pk_fma_f32 v[138:139], v[138:139], 2.0, 1.0 op_sel_hi:[1,0,0] neg_lo:[1,0,0] neg_hi:[1,0,0]
	v_add_u32_e32 v151, s1, v1
	v_cvt_pk_f16_f32 v138, v138, v139
	v_pk_fma_f32 v[146:147], v[146:147], 2.0, 1.0 op_sel_hi:[1,0,0] neg_lo:[1,0,0] neg_hi:[1,0,0]
	ds_write_b64 v151, v[148:149]
	v_cvt_pk_f16_f32 v139, v146, v147
	v_cvt_f32_f16_e32 v146, v140
	v_cvt_f32_f16_sdwa v140, v140 dst_sel:DWORD dst_unused:UNUSED_PAD src0_sel:WORD_1
	v_cvt_f32_f16_e32 v147, v141
	v_cvt_f32_f16_sdwa v141, v141 dst_sel:DWORD dst_unused:UNUSED_PAD src0_sel:WORD_1
	v_exp_f32_e32 v146, v146
	v_exp_f32_e32 v148, v140
	v_lshl_add_u32 v216, v153, 4, v152
	v_lshl_add_u32 v214, v154, 4, v152
	v_add_f32_e32 v140, 1.0, v146
	v_exp_f32_e32 v146, v147
	v_add_f32_e32 v147, 1.0, v148
	v_exp_f32_e32 v148, v141
	v_rcp_f32_e32 v141, v147
	v_add_f32_e32 v146, 1.0, v146
	v_rcp_f32_e32 v140, v140
	v_add_f32_e32 v147, 1.0, v148
	v_rcp_f32_e32 v146, v146
	v_rcp_f32_e32 v147, v147
	v_add_u32_e32 v148, s1, v216
	ds_write_b64 v148, v[138:139]
	v_pk_fma_f32 v[138:139], v[140:141], 2.0, 1.0 op_sel_hi:[1,0,0] neg_lo:[1,0,0] neg_hi:[1,0,0]
	v_pk_fma_f32 v[140:141], v[146:147], 2.0, 1.0 op_sel_hi:[1,0,0] neg_lo:[1,0,0] neg_hi:[1,0,0]
	v_cvt_pk_f16_f32 v138, v138, v139
	v_cvt_pk_f16_f32 v139, v140, v141
	v_add_u32_e32 v140, s1, v214
	s_lshl_b32 s2, s12, 7
	s_add_i32 s1, 0, 0x20000
	s_add_u32 s0, s4, s0
	ds_write_b64 v140, v[138:139]
	v_add_u32_e32 v219, s1, v143
	v_bitop3_b32 v138, v218, v0, 15 bitop3:0x78
	s_addc_u32 s1, s5, 0
	v_lshlrev_b32_e32 v220, 4, v138
	v_lshl_add_u64 v[138:139], s[0:1], 0, v[144:145]
	s_mov_b64 s[0:1], 0x800080
	s_waitcnt lgkmcnt(0)
	s_barrier
	v_lshl_add_u64 v[208:209], v[138:139], 0, s[0:1]
	s_waitcnt vmcnt(0)
	v_mov_b32_e32 v232, v170
	v_mov_b32_e32 v233, v171
	v_mov_b32_e32 v234, v172
	v_mov_b32_e32 v235, v173
	v_mov_b32_e32 v236, v202
	v_mov_b32_e32 v237, v203
	v_mov_b32_e32 v238, v204
	v_mov_b32_e32 v239, v205
	v_mov_b32_e32 v224, v178
	v_mov_b32_e32 v225, v179
	v_mov_b32_e32 v226, v180
	v_mov_b32_e32 v227, v181
	v_mov_b32_e32 v228, v174
	v_mov_b32_e32 v229, v175
	v_mov_b32_e32 v230, v176
	v_mov_b32_e32 v231, v177
	s_mov_b64 s[0:1], 0x400000
	v_xor_b32_e32 v221, 64, v220
	v_xor_b32_e32 v222, 0x80, v220
	v_xor_b32_e32 v223, 0xc0, v220
	ds_read_b128 v[154:157], v213 offset:0
	ds_read_b128 v[158:161], v213 offset:1024
	ds_read_b128 v[162:165], v213 offset:2048
	ds_read_b128 v[166:169], v213 offset:3072
	s_waitcnt lgkmcnt(0)
.Lrnn_top:
	s_add_i32 s4, s3, 0xffffc000
	s_and_b32 s4, s4, 0x4000
	s_and_b32 s5, s3, 0x4000
	s_add_i32 s5, s5, 0x20000
	v_add_u32_e32 v244, s4, v219
	v_add_u32_e32 v240, v244, v220
	v_add_u32_e32 v241, v244, v221
	v_add_u32_e32 v242, v244, v222
	v_add_u32_e32 v243, v244, v223
	ds_read_b128 v[138:141], v240 offset:0
	ds_read_b128 v[142:145], v241 offset:0
	ds_read_b128 v[146:149], v240 offset:256
	ds_read_b128 v[150:153], v240 offset:768
	s_waitcnt vmcnt(2)
	v_cvt_f32_f16_e32 v198, v224
	v_cvt_f32_f16_sdwa v199, v224 dst_sel:DWORD dst_unused:UNUSED_PAD src0_sel:WORD_1
	v_cvt_f32_f16_e32 v200, v225
	v_cvt_f32_f16_sdwa v201, v225 dst_sel:DWORD dst_unused:UNUSED_PAD src0_sel:WORD_1
	v_cvt_f32_f16_e32 v194, v226
	v_cvt_f32_f16_sdwa v195, v226 dst_sel:DWORD dst_unused:UNUSED_PAD src0_sel:WORD_1
	v_cvt_f32_f16_e32 v196, v227
	v_cvt_f32_f16_sdwa v197, v227 dst_sel:DWORD dst_unused:UNUSED_PAD src0_sel:WORD_1
	v_cvt_f32_f16_e32 v190, v228
	v_cvt_f32_f16_sdwa v191, v228 dst_sel:DWORD dst_unused:UNUSED_PAD src0_sel:WORD_1
	v_cvt_f32_f16_e32 v192, v229
	v_cvt_f32_f16_sdwa v193, v229 dst_sel:DWORD dst_unused:UNUSED_PAD src0_sel:WORD_1
	v_cvt_f32_f16_e32 v186, v230
	v_cvt_f32_f16_sdwa v187, v230 dst_sel:DWORD dst_unused:UNUSED_PAD src0_sel:WORD_1
	v_cvt_f32_f16_e32 v188, v231
	v_cvt_f32_f16_sdwa v189, v231 dst_sel:DWORD dst_unused:UNUSED_PAD src0_sel:WORD_1
	s_cmp_eq_u32 s3, 0x40000
	s_cbranch_scc1 .Lrnn_sk1
	global_load_dwordx4 v[224:227], v[208:209], off offset:-128
	global_load_dwordx4 v[228:231], v[208:209], off offset:-64

.Lrnn_sk2:
	v_mfma_f32_16x16x32_f16 v[186:189], a[124:127], v[146:149], v[186:189]
	ds_read_b128 v[146:149], v241 offset:512
	s_waitcnt lgkmcnt(3)
	v_mfma_f32_16x16x32_f16 v[198:201], v[154:157], v[150:153], v[198:201]
	ds_read_b128 v[154:157], v213 offset:8192
	v_mfma_f32_16x16x32_f16 v[194:197], v[158:161], v[150:153], v[194:197]
	ds_read_b128 v[158:161], v213 offset:9216
	v_mfma_f32_16x16x32_f16 v[190:193], v[162:165], v[150:153], v[190:193]
	ds_read_b128 v[162:165], v213 offset:10240
	v_mfma_f32_16x16x32_f16 v[186:189], v[166:169], v[150:153], v[186:189]
	ds_read_b128 v[166:169], v213 offset:11264
	ds_read_b128 v[150:153], v241 offset:768
	s_waitcnt lgkmcnt(7)
	v_mfma_f32_16x16x32_f16 v[198:201], a[140:143], v[138:141], v[198:201]
	v_mfma_f32_16x16x32_f16 v[194:197], a[144:147], v[138:141], v[194:197]
	v_mfma_f32_16x16x32_f16 v[190:193], a[148:151], v[138:141], v[190:193]
	v_mfma_f32_16x16x32_f16 v[186:189], a[168:171], v[138:141], v[186:189]
	ds_read_b128 v[138:141], v242 offset:0
	s_waitcnt lgkmcnt(7)
	v_mfma_f32_16x16x32_f16 v[198:201], v[10:13], v[142:145], v[198:201]
	v_mfma_f32_16x16x32_f16 v[194:197], v[14:17], v[142:145], v[194:197]
	v_mfma_f32_16x16x32_f16 v[190:193], v[18:21], v[142:145], v[190:193]
	v_mfma_f32_16x16x32_f16 v[186:189], v[22:25], v[142:145], v[186:189]
	ds_read_b128 v[142:145], v243 offset:0
	s_waitcnt lgkmcnt(7)
	v_mfma_f32_16x16x32_f16 v[198:201], v[54:57], v[146:149], v[198:201]
	v_mfma_f32_16x16x32_f16 v[194:197], v[58:61], v[146:149], v[194:197]
	v_mfma_f32_16x16x32_f16 v[190:193], v[62:65], v[146:149], v[190:193]
	v_mfma_f32_16x16x32_f16 v[186:189], v[66:69], v[146:149], v[186:189]
	ds_read_b128 v[146:149], v242 offset:256
	s_waitcnt lgkmcnt(3)
	v_mfma_f32_16x16x32_f16 v[198:201], v[154:157], v[150:153], v[198:201]
	ds_read_b128 v[154:157], v213 offset:16384
	v_mfma_f32_16x16x32_f16 v[194:197], v[158:161], v[150:153], v[194:197]
	ds_read_b128 v[158:161], v213 offset:17408
	v_mfma_f32_16x16x32_f16 v[190:193], v[162:165], v[150:153], v[190:193]
	ds_read_b128 v[162:165], v213 offset:18432
	v_mfma_f32_16x16x32_f16 v[186:189], v[166:169], v[150:153], v[186:189]
	ds_read_b128 v[166:169], v213 offset:19456
	ds_read_b128 v[150:153], v242 offset:768
	s_waitcnt lgkmcnt(7)
	v_mfma_f32_16x16x32_f16 v[198:201], a[48:51], v[138:141], v[198:201]
	v_mfma_f32_16x16x32_f16 v[194:197], a[52:55], v[138:141], v[194:197]
	v_mfma_f32_16x16x32_f16 v[190:193], a[56:59], v[138:141], v[190:193]
	v_mfma_f32_16x16x32_f16 v[186:189], a[60:63], v[138:141], v[186:189]
	ds_read_b128 v[138:141], v243 offset:256
	s_waitcnt lgkmcnt(7)
	v_mfma_f32_16x16x32_f16 v[198:201], a[76:79], v[142:145], v[198:201]
	v_mfma_f32_16x16x32_f16 v[194:197], a[80:83], v[142:145], v[194:197]
	v_mfma_f32_16x16x32_f16 v[190:193], a[84:87], v[142:145], v[190:193]
	v_mfma_f32_16x16x32_f16 v[186:189], a[88:91], v[142:145], v[186:189]
	ds_read_b128 v[142:145], v242 offset:512
	s_waitcnt lgkmcnt(7)
	v_mfma_f32_16x16x32_f16 v[198:201], a[176:179], v[146:149], v[198:201]
	v_mfma_f32_16x16x32_f16 v[194:197], a[180:183], v[146:149], v[194:197]
	v_mfma_f32_16x16x32_f16 v[190:193], a[184:187], v[146:149], v[190:193]
	v_mfma_f32_16x16x32_f16 v[186:189], a[188:191], v[146:149], v[186:189]
	ds_read_b128 v[146:149], v243 offset:512
	s_waitcnt lgkmcnt(3)
	v_mfma_f32_16x16x32_f16 v[198:201], v[154:157], v[150:153], v[198:201]
	ds_read_b128 v[154:157], v213 offset:24576
	v_mfma_f32_16x16x32_f16 v[194:197], v[158:161], v[150:153], v[194:197]
	ds_read_b128 v[158:161], v213 offset:25600
	v_mfma_f32_16x16x32_f16 v[190:193], v[162:165], v[150:153], v[190:193]
	ds_read_b128 v[162:165], v213 offset:26624
	v_mfma_f32_16x16x32_f16 v[186:189], v[166:169], v[150:153], v[186:189]
	ds_read_b128 v[166:169], v213 offset:27648
	ds_read_b128 v[150:153], v243 offset:768
	s_waitcnt lgkmcnt(7)
	v_mfma_f32_16x16x32_f16 v[198:201], a[212:215], v[138:141], v[198:201]
	v_mfma_f32_16x16x32_f16 v[194:197], a[216:219], v[138:141], v[194:197]
	v_mfma_f32_16x16x32_f16 v[190:193], a[220:223], v[138:141], v[190:193]
	v_mfma_f32_16x16x32_f16 v[186:189], a[232:235], v[138:141], v[186:189]
	ds_read_b128 v[138:141], v240 offset:0
	s_waitcnt lgkmcnt(7)
	v_mfma_f32_16x16x32_f16 v[198:201], v[74:77], v[142:145], v[198:201]
	v_mfma_f32_16x16x32_f16 v[194:197], v[78:81], v[142:145], v[194:197]
	v_mfma_f32_16x16x32_f16 v[190:193], v[82:85], v[142:145], v[190:193]
	v_mfma_f32_16x16x32_f16 v[186:189], v[86:89], v[142:145], v[186:189]
	ds_read_b128 v[142:145], v241 offset:0
	s_waitcnt lgkmcnt(7)
	v_mfma_f32_16x16x32_f16 v[198:201], v[94:97], v[146:149], v[198:201]
	v_mfma_f32_16x16x32_f16 v[194:197], v[98:101], v[146:149], v[194:197]
	v_mfma_f32_16x16x32_f16 v[190:193], v[102:105], v[146:149], v[190:193]
	v_mfma_f32_16x16x32_f16 v[186:189], v[106:109], v[146:149], v[186:189]
	ds_read_b128 v[146:149], v240 offset:256
	s_waitcnt lgkmcnt(3)
	v_mfma_f32_16x16x32_f16 v[198:201], v[154:157], v[150:153], v[198:201]
	ds_read_b128 v[154:157], v213 offset:4096
	v_mfma_f32_16x16x32_f16 v[194:197], v[158:161], v[150:153], v[194:197]
	ds_read_b128 v[158:161], v213 offset:5120
	v_mfma_f32_16x16x32_f16 v[190:193], v[162:165], v[150:153], v[190:193]
	ds_read_b128 v[162:165], v213 offset:6144
	v_mfma_f32_16x16x32_f16 v[186:189], v[166:169], v[150:153], v[186:189]
	ds_read_b128 v[166:169], v213 offset:7168
	ds_read_b128 v[150:153], v240 offset:768
	s_waitcnt lgkmcnt(7)
	v_mfma_f32_16x16x32_f16 v[182:185], a[8:11], v[138:141], v[182:185]
	v_mfma_f32_16x16x32_f16 v[178:181], a[0:3], v[138:141], v[178:181]
	v_mfma_f32_16x16x32_f16 v[174:177], a[4:7], v[138:141], v[174:177]
	v_mfma_f32_16x16x32_f16 v[170:173], a[32:35], v[138:141], v[170:173]
	ds_read_b128 v[138:141], v241 offset:256
	s_waitcnt lgkmcnt(7)
	v_mfma_f32_16x16x32_f16 v[182:185], a[28:31], v[142:145], v[182:185]
	v_exp_f32_e32 v198, v198
	v_mfma_f32_16x16x32_f16 v[178:181], a[36:39], v[142:145], v[178:181]
	v_exp_f32_e32 v199, v199
	v_mfma_f32_16x16x32_f16 v[174:177], a[40:43], v[142:145], v[174:177]
	v_exp_f32_e32 v200, v200
	v_mfma_f32_16x16x32_f16 v[170:173], a[44:47], v[142:145], v[170:173]
	ds_read_b128 v[142:145], v240 offset:512
	v_exp_f32_e32 v201, v201
	s_waitcnt lgkmcnt(7)
	v_mfma_f32_16x16x32_f16 v[182:185], a[136:139], v[146:149], v[182:185]
	v_exp_f32_e32 v194, v194
	v_mfma_f32_16x16x32_f16 v[178:181], a[128:131], v[146:149], v[178:181]
	v_exp_f32_e32 v195, v195
	v_mfma_f32_16x16x32_f16 v[174:177], a[132:135], v[146:149], v[174:177]
	v_exp_f32_e32 v196, v196
	v_mfma_f32_16x16x32_f16 v[170:173], a[152:155], v[146:149], v[170:173]
	ds_read_b128 v[146:149], v241 offset:512
	v_exp_f32_e32 v197, v197
	s_waitcnt lgkmcnt(3)
	v_mfma_f32_16x16x32_f16 v[182:185], v[154:157], v[150:153], v[182:185]
	ds_read_b128 v[154:157], v213 offset:12288
	v_exp_f32_e32 v190, v190
	v_mfma_f32_16x16x32_f16 v[178:181], v[158:161], v[150:153], v[178:181]
	ds_read_b128 v[158:161], v213 offset:13312
	v_exp_f32_e32 v191, v191
	v_mfma_f32_16x16x32_f16 v[174:177], v[162:165], v[150:153], v[174:177]
	ds_read_b128 v[162:165], v213 offset:14336
	v_exp_f32_e32 v192, v192
	v_mfma_f32_16x16x32_f16 v[170:173], v[166:169], v[150:153], v[170:173]
	ds_read_b128 v[166:169], v213 offset:15360
	ds_read_b128 v[150:153], v241 offset:768
	v_exp_f32_e32 v193, v193
	s_waitcnt lgkmcnt(7)
	v_mfma_f32_16x16x32_f16 v[182:185], a[172:175], v[138:141], v[182:185]
	v_exp_f32_e32 v186, v186
	v_mfma_f32_16x16x32_f16 v[178:181], a[156:159], v[138:141], v[178:181]
	v_exp_f32_e32 v187, v187
	v_mfma_f32_16x16x32_f16 v[174:177], a[160:163], v[138:141], v[174:177]
	v_exp_f32_e32 v188, v188
	v_mfma_f32_16x16x32_f16 v[170:173], a[164:167], v[138:141], v[170:173]
	ds_read_b128 v[138:141], v242 offset:0
	v_exp_f32_e32 v189, v189
	s_waitcnt lgkmcnt(7)
	v_mfma_f32_16x16x32_f16 v[182:185], v[50:53], v[142:145], v[182:185]
	v_pk_add_f32 v[198:199], v[198:199], 1.0 op_sel_hi:[1,0]
	v_mfma_f32_16x16x32_f16 v[178:181], v[26:29], v[142:145], v[178:181]
	v_pk_add_f32 v[200:201], v[200:201], 1.0 op_sel_hi:[1,0]
	v_mfma_f32_16x16x32_f16 v[174:177], v[30:33], v[142:145], v[174:177]
	v_pk_add_f32 v[194:195], v[194:195], 1.0 op_sel_hi:[1,0]
	v_mfma_f32_16x16x32_f16 v[170:173], v[34:37], v[142:145], v[170:173]
	ds_read_b128 v[142:145], v243 offset:0
	v_pk_add_f32 v[196:197], v[196:197], 1.0 op_sel_hi:[1,0]
	s_waitcnt lgkmcnt(7)
	v_mfma_f32_16x16x32_f16 v[182:185], v[70:73], v[146:149], v[182:185]
	v_pk_add_f32 v[190:191], v[190:191], 1.0 op_sel_hi:[1,0]
	v_mfma_f32_16x16x32_f16 v[178:181], v[38:41], v[146:149], v[178:181]
	v_pk_add_f32 v[192:193], v[192:193], 1.0 op_sel_hi:[1,0]
	v_mfma_f32_16x16x32_f16 v[174:177], v[42:45], v[146:149], v[174:177]
	v_pk_add_f32 v[186:187], v[186:187], 1.0 op_sel_hi:[1,0]
	v_mfma_f32_16x16x32_f16 v[170:173], v[46:49], v[146:149], v[170:173]
	ds_read_b128 v[146:149], v242 offset:256
	v_pk_add_f32 v[188:189], v[188:189], 1.0 op_sel_hi:[1,0]
	s_waitcnt lgkmcnt(3)
	v_mfma_f32_16x16x32_f16 v[182:185], v[154:157], v[150:153], v[182:185]
	ds_read_b128 v[154:157], v213 offset:20480
	v_rcp_f32_e32 v198, v198
	v_mfma_f32_16x16x32_f16 v[178:181], v[158:161], v[150:153], v[178:181]
	ds_read_b128 v[158:161], v213 offset:21504
	v_rcp_f32_e32 v199, v199
	v_mfma_f32_16x16x32_f16 v[174:177], v[162:165], v[150:153], v[174:177]
	ds_read_b128 v[162:165], v213 offset:22528
	v_rcp_f32_e32 v200, v200
	v_mfma_f32_16x16x32_f16 v[170:173], v[166:169], v[150:153], v[170:173]
	ds_read_b128 v[166:169], v213 offset:23552
	ds_read_b128 v[150:153], v242 offset:768
	v_rcp_f32_e32 v201, v201
	s_waitcnt lgkmcnt(7)
	v_mfma_f32_16x16x32_f16 v[182:185], a[72:75], v[138:141], v[182:185]
	v_rcp_f32_e32 v194, v194
	v_mfma_f32_16x16x32_f16 v[178:181], a[64:67], v[138:141], v[178:181]
	v_rcp_f32_e32 v195, v195
	v_mfma_f32_16x16x32_f16 v[174:177], a[68:71], v[138:141], v[174:177]
	v_rcp_f32_e32 v196, v196
	v_mfma_f32_16x16x32_f16 v[170:173], a[96:99], v[138:141], v[170:173]
	ds_read_b128 v[138:141], v243 offset:256
	v_rcp_f32_e32 v197, v197
	s_waitcnt lgkmcnt(7)
	v_mfma_f32_16x16x32_f16 v[182:185], a[92:95], v[142:145], v[182:185]
	v_rcp_f32_e32 v190, v190
	v_mfma_f32_16x16x32_f16 v[178:181], a[100:103], v[142:145], v[178:181]
	v_rcp_f32_e32 v191, v191
	v_mfma_f32_16x16x32_f16 v[174:177], a[104:107], v[142:145], v[174:177]
	v_rcp_f32_e32 v192, v192
	v_mfma_f32_16x16x32_f16 v[170:173], a[108:111], v[142:145], v[170:173]
	ds_read_b128 v[142:145], v242 offset:512
	v_rcp_f32_e32 v193, v193
	s_waitcnt lgkmcnt(7)
	v_mfma_f32_16x16x32_f16 v[182:185], a[208:211], v[146:149], v[182:185]
	v_rcp_f32_e32 v186, v186
	v_mfma_f32_16x16x32_f16 v[178:181], a[224:227], v[146:149], v[178:181]
	v_rcp_f32_e32 v187, v187
	v_mfma_f32_16x16x32_f16 v[174:177], a[228:231], v[146:149], v[174:177]
	v_rcp_f32_e32 v188, v188
	v_mfma_f32_16x16x32_f16 v[170:173], a[240:243], v[146:149], v[170:173]
	ds_read_b128 v[146:149], v243 offset:512
	v_rcp_f32_e32 v189, v189
	s_waitcnt lgkmcnt(3)
	v_mfma_f32_16x16x32_f16 v[182:185], v[154:157], v[150:153], v[182:185]
	ds_read_b128 v[154:157], v213 offset:28672
	v_pk_fma_f32 v[198:199], v[198:199], 2.0, 1.0 op_sel_hi:[1,0,0] neg_lo:[1,0,0] neg_hi:[1,0,0]
	v_mfma_f32_16x16x32_f16 v[178:181], v[158:161], v[150:153], v[178:181]
	ds_read_b128 v[158:161], v213 offset:29696
	v_pk_fma_f32 v[200:201], v[200:201], 2.0, 1.0 op_sel_hi:[1,0,0] neg_lo:[1,0,0] neg_hi:[1,0,0]
	v_mfma_f32_16x16x32_f16 v[174:177], v[162:165], v[150:153], v[174:177]
	ds_read_b128 v[162:165], v213 offset:30720
	v_pk_fma_f32 v[194:195], v[194:195], 2.0, 1.0 op_sel_hi:[1,0,0] neg_lo:[1,0,0] neg_hi:[1,0,0]
	v_mfma_f32_16x16x32_f16 v[170:173], v[166:169], v[150:153], v[170:173]
	ds_read_b128 v[166:169], v213 offset:31744
	ds_read_b128 v[150:153], v243 offset:768
	v_pk_fma_f32 v[196:197], v[196:197], 2.0, 1.0 op_sel_hi:[1,0,0] neg_lo:[1,0,0] neg_hi:[1,0,0]
	s_waitcnt lgkmcnt(7)
	v_mfma_f32_16x16x32_f16 v[182:185], a[236:239], v[138:141], v[182:185]
	v_pk_fma_f32 v[190:191], v[190:191], 2.0, 1.0 op_sel_hi:[1,0,0] neg_lo:[1,0,0] neg_hi:[1,0,0]
	v_mfma_f32_16x16x32_f16 v[178:181], a[244:247], v[138:141], v[178:181]
	v_pk_fma_f32 v[192:193], v[192:193], 2.0, 1.0 op_sel_hi:[1,0,0] neg_lo:[1,0,0] neg_hi:[1,0,0]
	v_mfma_f32_16x16x32_f16 v[174:177], v[2:5], v[138:141], v[174:177]
	v_pk_fma_f32 v[186:187], v[186:187], 2.0, 1.0 op_sel_hi:[1,0,0] neg_lo:[1,0,0] neg_hi:[1,0,0]
	v_mfma_f32_16x16x32_f16 v[170:173], v[6:9], v[138:141], v[170:173]
	v_pk_fma_f32 v[188:189], v[188:189], 2.0, 1.0 op_sel_hi:[1,0,0] neg_lo:[1,0,0] neg_hi:[1,0,0]
	s_waitcnt lgkmcnt(6)
	v_mfma_f32_16x16x32_f16 v[182:185], v[90:93], v[142:145], v[182:185]
	v_cvt_pk_f16_f32 v198, v198, v199
	v_cvt_pk_f16_f32 v199, v200, v201
	v_mfma_f32_16x16x32_f16 v[178:181], v[114:117], v[142:145], v[178:181]
	v_cvt_pk_f16_f32 v194, v194, v195
	v_cvt_pk_f16_f32 v195, v196, v197
	v_mfma_f32_16x16x32_f16 v[174:177], v[118:121], v[142:145], v[174:177]
	v_cvt_pk_f16_f32 v190, v190, v191
	v_cvt_pk_f16_f32 v191, v192, v193
	v_mfma_f32_16x16x32_f16 v[170:173], v[122:125], v[142:145], v[170:173]
	v_cvt_pk_f16_f32 v186, v186, v187
	v_cvt_pk_f16_f32 v187, v188, v189
	s_waitcnt lgkmcnt(5)
	v_mfma_f32_16x16x32_f16 v[182:185], v[110:113], v[146:149], v[182:185]
	v_add_u32_e32 v244, s5, v217
	v_mfma_f32_16x16x32_f16 v[178:181], v[126:129], v[146:149], v[178:181]
	ds_write_b64 v244, v[198:199]
	v_mfma_f32_16x16x32_f16 v[174:177], v[130:133], v[146:149], v[174:177]
	v_add_u32_e32 v245, s5, v215
	v_mfma_f32_16x16x32_f16 v[170:173], v[134:137], v[146:149], v[170:173]
	ds_write_b64 v245, v[194:195]
	s_waitcnt lgkmcnt(2)
	v_mfma_f32_16x16x32_f16 v[182:185], v[154:157], v[150:153], v[182:185]
	v_add_u32_e32 v246, s5, v211
	v_mfma_f32_16x16x32_f16 v[178:181], v[158:161], v[150:153], v[178:181]
	ds_write_b64 v246, v[190:191]
	v_mfma_f32_16x16x32_f16 v[174:177], v[162:165], v[150:153], v[174:177]
	v_add_u32_e32 v247, s5, v212
	v_mfma_f32_16x16x32_f16 v[170:173], v[166:169], v[150:153], v[170:173]
	ds_write_b64 v247, v[186:187]
	ds_read_b128 v[154:157], v213 offset:0
	ds_read_b128 v[158:161], v213 offset:1024
	ds_read_b128 v[162:165], v213 offset:2048
	ds_read_b128 v[166:169], v213 offset:3072
	v_exp_f32_e32 v182, v182
	v_exp_f32_e32 v183, v183
	v_exp_f32_e32 v184, v184
	v_exp_f32_e32 v185, v185
	v_exp_f32_e32 v178, v178
	v_exp_f32_e32 v179, v179
	v_exp_f32_e32 v180, v180
	v_exp_f32_e32 v181, v181
	v_exp_f32_e32 v174, v174
	v_exp_f32_e32 v175, v175
	v_exp_f32_e32 v176, v176
	v_exp_f32_e32 v177, v177
	v_exp_f32_e32 v170, v170
	v_exp_f32_e32 v171, v171
	v_exp_f32_e32 v172, v172
	v_exp_f32_e32 v173, v173
	v_pk_add_f32 v[182:183], v[182:183], 1.0 op_sel_hi:[1,0]
	v_pk_add_f32 v[184:185], v[184:185], 1.0 op_sel_hi:[1,0]
	v_pk_add_f32 v[178:179], v[178:179], 1.0 op_sel_hi:[1,0]
	v_pk_add_f32 v[180:181], v[180:181], 1.0 op_sel_hi:[1,0]
	v_pk_add_f32 v[174:175], v[174:175], 1.0 op_sel_hi:[1,0]
	v_pk_add_f32 v[176:177], v[176:177], 1.0 op_sel_hi:[1,0]
	v_pk_add_f32 v[170:171], v[170:171], 1.0 op_sel_hi:[1,0]
	v_pk_add_f32 v[172:173], v[172:173], 1.0 op_sel_hi:[1,0]
	v_rcp_f32_e32 v182, v182
	v_rcp_f32_e32 v183, v183
	v_rcp_f32_e32 v184, v184
	v_rcp_f32_e32 v185, v185
	v_rcp_f32_e32 v178, v178
	v_rcp_f32_e32 v179, v179
	v_rcp_f32_e32 v180, v180
	v_rcp_f32_e32 v181, v181
	v_rcp_f32_e32 v174, v174
	v_rcp_f32_e32 v175, v175
	v_rcp_f32_e32 v176, v176
	v_rcp_f32_e32 v177, v177
	v_rcp_f32_e32 v170, v170
	v_rcp_f32_e32 v171, v171
	v_rcp_f32_e32 v172, v172
	v_rcp_f32_e32 v173, v173
	v_pk_fma_f32 v[182:183], v[182:183], 2.0, 1.0 op_sel_hi:[1,0,0] neg_lo:[1,0,0] neg_hi:[1,0,0]
	v_pk_fma_f32 v[184:185], v[184:185], 2.0, 1.0 op_sel_hi:[1,0,0] neg_lo:[1,0,0] neg_hi:[1,0,0]
	v_pk_fma_f32 v[178:179], v[178:179], 2.0, 1.0 op_sel_hi:[1,0,0] neg_lo:[1,0,0] neg_hi:[1,0,0]
	v_pk_fma_f32 v[180:181], v[180:181], 2.0, 1.0 op_sel_hi:[1,0,0] neg_lo:[1,0,0] neg_hi:[1,0,0]
	v_pk_fma_f32 v[174:175], v[174:175], 2.0, 1.0 op_sel_hi:[1,0,0] neg_lo:[1,0,0] neg_hi:[1,0,0]
	v_pk_fma_f32 v[176:177], v[176:177], 2.0, 1.0 op_sel_hi:[1,0,0] neg_lo:[1,0,0] neg_hi:[1,0,0]
	v_pk_fma_f32 v[170:171], v[170:171], 2.0, 1.0 op_sel_hi:[1,0,0] neg_lo:[1,0,0] neg_hi:[1,0,0]
	v_pk_fma_f32 v[172:173], v[172:173], 2.0, 1.0 op_sel_hi:[1,0,0] neg_lo:[1,0,0] neg_hi:[1,0,0]
	v_cvt_pk_f16_f32 v182, v182, v183
	v_cvt_pk_f16_f32 v183, v184, v185
	v_cvt_pk_f16_f32 v178, v178, v179
	v_cvt_pk_f16_f32 v179, v180, v181
	v_cvt_pk_f16_f32 v174, v174, v175
	v_cvt_pk_f16_f32 v175, v176, v177
	v_cvt_pk_f16_f32 v170, v170, v171
	v_cvt_pk_f16_f32 v171, v172, v173
	v_add_u32_e32 v244, s5, v210
	ds_write_b64 v244, v[182:183]
	v_add_u32_e32 v245, s5, v1
	ds_write_b64 v245, v[178:179]
	v_add_u32_e32 v246, s5, v216
	ds_write_b64 v246, v[174:175]
	v_add_u32_e32 v247, s5, v214
	ds_write_b64 v247, v[170:171]
	s_addk_i32 s3, 0x4000
	v_lshl_add_u64 v[208:209], v[208:209], 0, s[0:1]
	s_cmp_eq_u32 s3, 0x44000
	s_waitcnt lgkmcnt(0)
	s_barrier
	s_cbranch_scc0 .Lrnn_top

.LBB8_5:
	s_ashr_i32 s28, s7, 3
	v_lshlrev_b32_e32 v2, 9, v178
	s_movk_i32 s7, 0x1e00
	v_and_or_b32 v2, v2, s7, v177
	v_lshlrev_b32_e32 v183, 1, v2
	v_mul_lo_u32 v2, s6, v182
	v_add_lshl_u32 v162, v2, v177, 1
	v_lshlrev_b32_e32 v2, 6, v181
	s_movk_i32 s7, 0xc00
	s_lshl_b32 s43, s26, 3
	v_and_or_b32 v184, v2, s7, v176
	v_mul_lo_u32 v2, s6, v180
	s_abs_i32 s44, s43
	v_add_lshl_u32 v164, v2, v177, 1
	v_cvt_f32_u32_e32 v2, s44
	s_sub_i32 s29, 0, s44
	s_add_i32 s27, s27, s28
	s_ashr_i32 s28, s27, 31
	v_rcp_iflag_f32_e32 v2, v2
	s_bfe_i32 s46, s26, 0x1001c
	s_xor_b32 s26, s28, s46
	s_abs_i32 s28, s27
	v_mul_f32_e32 v2, 0x4f7ffffe, v2
	v_cvt_u32_f32_e32 v2, v2
	s_lshr_b32 s36, s19, 6
	s_ashr_i32 s7, s6, 31
	s_lshr_b32 s37, s19, 8
	v_readfirstlane_b32 s47, v2
	s_mul_i32 s29, s29, s47
	s_mul_hi_u32 s29, s47, s29
	s_add_i32 s47, s47, s29
	s_mul_hi_u32 s29, s28, s47
	s_mul_i32 s30, s29, s44
	s_sub_i32 s28, s28, s30
	s_lshl_b64 s[22:23], s[6:7], 8
	s_lshl_b64 s[24:25], s[6:7], 9
	s_lshl_b32 s45, s36, 10
	s_add_i32 s30, s29, 1
	s_sub_i32 s31, s28, s44
	s_cmp_ge_u32 s28, s44
	s_cselect_b32 s29, s30, s29
	s_cselect_b32 s28, s31, s28
	s_add_i32 s30, s29, 1
	s_cmp_ge_u32 s28, s44
	s_cselect_b32 s28, s30, s29
	s_xor_b32 s28, s28, s26
	s_sub_i32 s26, s28, s26
	s_lshl_b32 s28, s26, 3
	s_sub_i32 s29, s33, s28
	s_min_i32 s29, s29, 8
	s_abs_i32 s30, s29
	v_cvt_f32_u32_e32 v2, s30
	s_sub_i32 s34, 0, s30
	s_mul_i32 s26, s26, s43
	v_lshlrev_b32_e32 v3, 6, v179
	v_rcp_iflag_f32_e32 v2, v2
	s_movk_i32 s31, 0x1c00
	s_sub_i32 s26, s27, s26
	v_and_or_b32 v185, v3, s31, v176
	v_mul_f32_e32 v2, 0x4f7ffffe, v2
	v_cvt_u32_f32_e32 v2, v2
	s_abs_i32 s31, s26
	s_xor_b32 s27, s26, s29
	s_ashr_i32 s27, s27, 31
	v_readfirstlane_b32 s35, v2
	s_mul_i32 s34, s34, s35
	s_mul_hi_u32 s34, s35, s34
	s_add_i32 s35, s35, s34
	s_mul_hi_u32 s34, s31, s35
	s_mul_i32 s35, s34, s30
	s_sub_i32 s31, s31, s35
	s_add_i32 s35, s34, 1
	s_sub_i32 s48, s31, s30
	s_cmp_ge_u32 s31, s30
	s_cselect_b32 s34, s35, s34
	s_cselect_b32 s31, s48, s31
	s_add_i32 s35, s34, 1
	s_cmp_ge_u32 s31, s30
	s_cselect_b32 s30, s35, s34
	s_xor_b32 s30, s30, s27
	s_sub_i32 s58, s30, s27
	s_mul_i32 s27, s58, s29
	s_sub_i32 s26, s26, s27
	s_add_i32 s57, s26, s28
	s_ashr_i32 s26, s58, 31
	s_mul_i32 s26, s24, s26
	s_mul_hi_u32 s27, s24, s58
	s_add_i32 s28, s27, s26
	s_lshr_b64 s[26:27], s[6:7], 23
	s_mul_i32 s26, s26, s58
	s_add_i32 s28, s28, s26
	s_mul_i32 s26, s24, s58
	s_waitcnt lgkmcnt(0)
	s_add_u32 s34, s20, s26
	s_addc_u32 s35, s21, s28
	s_lshl_b32 s26, s57, 13
	s_ashr_i32 s27, s26, 31
	s_lshl_b64 s[26:27], s[26:27], 1
	s_add_u32 s28, s8, s26
	s_addc_u32 s29, s9, s27
	s_lshl_b32 s26, s57, 14
	s_ashr_i32 s27, s26, 31
	s_lshl_b64 s[26:27], s[26:27], 1
	s_add_u32 s30, s10, s26
	s_addc_u32 s31, s11, s27
	s_nop 4
	global_load_dwordx4 v[26:29], v184, s[28:29]
	global_load_dwordx4 v[30:33], v185, s[28:29]
	s_add_i32 s52, s45, 0
	global_load_dwordx4 v[34:37], v183, s[30:31]
	s_add_i32 m0, s52, 0x10000
	v_mov_b32_e32 v163, 0
	global_load_lds_dwordx4 v162, s[34:35]
	s_add_i32 m0, s52, 0x12000
	v_mov_b32_e32 v2, v163
	global_load_lds_dwordx4 v164, s[34:35]
	v_mov_b32_e32 v3, v163
	v_mov_b32_e32 v4, v163
	v_mov_b32_e32 v5, v163
	s_add_u32 s26, s28, 0x2000
	s_addc_u32 s27, s29, 0
	v_add_u32_e32 v186, 0, v1
	s_add_u32 s48, s30, 0x4000
	s_addc_u32 s49, s31, 0
	s_nop 4
	global_load_dwordx4 v[38:41], v184, s[26:27]
	global_load_dwordx4 v[42:45], v185, s[26:27]
	global_load_dwordx4 v[46:49], v183, s[48:49]
	s_add_u32 s26, s34, s22
	s_addc_u32 s27, s35, s23
	s_add_i32 m0, s52, 0x14000
	v_mov_b32_e32 v165, v163
	global_load_lds_dwordx4 v162, s[26:27]
	s_add_i32 m0, s52, 0x16000
	s_add_u32 s48, s28, 0x80
	s_addc_u32 s49, s29, 0
	global_load_lds_dwordx4 v164, s[26:27]
	s_add_u32 s50, s30, 0x80
	s_addc_u32 s51, s31, 0
	s_nop 4
	global_load_dwordx4 v[50:53], v184, s[48:49]
	v_lshl_add_u64 v[18:19], s[34:35], 0, v[162:163]
	v_lshl_add_u64 v[22:23], s[26:27], 0, v[162:163]
	v_lshl_add_u64 v[24:25], s[26:27], 0, v[164:165]
	s_mov_b64 s[26:27], 0x80
	global_load_dwordx4 v[54:57], v185, s[48:49]
	v_lshl_add_u64 v[20:21], s[34:35], 0, v[164:165]
	global_load_dwordx4 v[58:61], v183, s[50:51]
	s_add_i32 m0, s52, 0x18000
	v_lshl_add_u64 v[18:19], v[18:19], 0, s[26:27]
	global_load_lds_dwordx4 v[18:19], off
	v_lshl_add_u64 v[18:19], v[20:21], 0, s[26:27]
	s_add_i32 m0, s52, 0x1a000
	s_add_u32 s28, s28, 0x2080
	s_addc_u32 s29, s29, 0
	global_load_lds_dwordx4 v[18:19], off
	s_add_u32 s30, s30, 0x4080
	s_addc_u32 s31, s31, 0
	s_nop 4
	global_load_dwordx4 v[14:17], v184, s[28:29]
	global_load_dwordx4 v[6:9], v185, s[28:29]
	global_load_dwordx4 v[10:13], v183, s[30:31]
	s_add_i32 m0, s52, 0x1c000
	v_lshl_add_u64 v[18:19], v[22:23], 0, s[26:27]
	global_load_lds_dwordx4 v[18:19], off
	v_lshl_add_u64 v[18:19], v[24:25], 0, s[26:27]
	s_add_i32 m0, s52, 0x1e000
	s_load_dword s29, s[0:1], 0x60
	global_load_lds_dwordx4 v[18:19], off
	s_waitcnt vmcnt(17)
	v_pk_add_f16 v26, v26, v34
	v_pk_add_f16 v27, v27, v35
	v_pk_add_f16 v28, v28, v36
	v_pk_add_f16 v29, v29, v37
	v_pk_max_f16 v26, v26, 0
	v_pk_max_f16 v27, v27, 0
	v_pk_max_f16 v28, v28, 0
	v_pk_max_f16 v29, v29, 0
	v_pk_add_f16 v30, v30, v34
	v_pk_add_f16 v31, v31, v35
	v_pk_add_f16 v32, v32, v36
	v_pk_add_f16 v33, v33, v37
	v_pk_max_f16 v30, v30, 0
	v_pk_max_f16 v31, v31, 0
	v_pk_max_f16 v32, v32, 0
	v_pk_max_f16 v33, v33, 0
	ds_write_b128 v186, v[26:29]
	ds_write_b128 v186, v[30:33] offset:8192
	s_waitcnt vmcnt(12)
	v_pk_add_f16 v38, v38, v46
	v_pk_add_f16 v39, v39, v47
	v_pk_add_f16 v40, v40, v48
	v_pk_add_f16 v41, v41, v49
	v_pk_max_f16 v38, v38, 0
	v_pk_max_f16 v39, v39, 0
	v_pk_max_f16 v40, v40, 0
	v_pk_max_f16 v41, v41, 0
	v_pk_add_f16 v42, v42, v46
	v_pk_add_f16 v43, v43, v47
	v_pk_add_f16 v44, v44, v48
	v_pk_add_f16 v45, v45, v49
	v_pk_max_f16 v42, v42, 0
	v_pk_max_f16 v43, v43, 0
	v_pk_max_f16 v44, v44, 0
	v_pk_max_f16 v45, v45, 0
	ds_write_b128 v186, v[38:41] offset:16384
	ds_write_b128 v186, v[42:45] offset:24576
	s_waitcnt vmcnt(7)
	v_pk_add_f16 v50, v50, v58
	v_pk_add_f16 v51, v51, v59
	v_pk_add_f16 v52, v52, v60
	v_pk_add_f16 v53, v53, v61
	v_pk_max_f16 v50, v50, 0
	v_pk_max_f16 v51, v51, 0
	v_pk_max_f16 v52, v52, 0
	v_pk_max_f16 v53, v53, 0
	v_pk_add_f16 v54, v54, v58
	v_pk_add_f16 v55, v55, v59
	v_pk_add_f16 v56, v56, v60
	v_pk_add_f16 v57, v57, v61
	v_pk_max_f16 v54, v54, 0
	v_pk_max_f16 v55, v55, 0
	v_pk_max_f16 v56, v56, 0
	v_pk_max_f16 v57, v57, 0
	ds_write_b128 v186, v[50:53] offset:32768
	ds_write_b128 v186, v[54:57] offset:40960
	s_cmp_lg_u32 s37, 1
	s_mov_b32 s48, 0
	s_cbranch_scc1 .LBB8_7
	s_barrier

.LBB8_30:
	v_lshlrev_b32_e32 v2, 10, v178
	s_movk_i32 s5, 0x1c00
	v_and_b32_e32 v0, 8, v178
	v_and_or_b32 v2, v2, s5, v177
	s_movk_i32 s5, 0x70
	s_lshl_b32 s42, s6, 3
	v_and_or_b32 v3, v181, 48, v0
	v_and_or_b32 v0, v179, s5, v0
	s_abs_i32 s43, s42
	v_lshl_or_b32 v170, v0, 7, v176
	v_cvt_f32_u32_e32 v0, s43
	s_add_i32 s4, s7, s4
	s_sub_i32 s7, 0, s43
	s_bfe_i32 s45, s6, 0x1001c
	v_rcp_iflag_f32_e32 v0, v0
	s_abs_i32 s6, s4
	s_lshr_b32 s26, s36, 6
	s_ashr_i32 s19, s18, 31
	v_mul_f32_e32 v0, 0x4f7ffffe, v0
	v_cvt_u32_f32_e32 v0, v0
	s_ashr_i32 s5, s4, 31
	s_lshr_b32 s27, s36, 8
	s_lshl_b64 s[14:15], s[18:19], 8
	v_readfirstlane_b32 s46, v0
	s_mul_i32 s7, s7, s46
	s_mul_hi_u32 s7, s46, s7
	s_add_i32 s46, s46, s7
	s_mul_hi_u32 s7, s6, s46
	s_mul_i32 s20, s7, s43
	s_sub_i32 s6, s6, s20
	s_lshl_b64 s[16:17], s[18:19], 9
	s_lshl_b32 s44, s26, 10
	s_xor_b32 s5, s5, s45
	s_add_i32 s20, s7, 1
	s_sub_i32 s21, s6, s43
	s_cmp_ge_u32 s6, s43
	s_cselect_b32 s7, s20, s7
	s_cselect_b32 s6, s21, s6
	s_add_i32 s20, s7, 1
	s_cmp_ge_u32 s6, s43
	s_cselect_b32 s6, s20, s7
	s_xor_b32 s6, s6, s5
	s_sub_i32 s5, s6, s5
	s_lshl_b32 s6, s5, 3
	s_sub_i32 s7, s33, s6
	s_min_i32 s7, s7, 8
	s_abs_i32 s20, s7
	v_cvt_f32_u32_e32 v0, s20
	s_sub_i32 s24, 0, s20
	s_mul_i32 s5, s5, s42
	s_movk_i32 s21, 0x2000
	v_rcp_iflag_f32_e32 v0, v0
	s_sub_i32 s4, s4, s5
	v_lshlrev_b32_e32 v169, 1, v2
	v_and_or_b32 v2, v175, s21, v2
	v_mul_f32_e32 v0, 0x4f7ffffe, v0
	v_cvt_u32_f32_e32 v0, v0
	s_abs_i32 s21, s4
	s_xor_b32 s5, s4, s7
	s_ashr_i32 s5, s5, 31
	v_readfirstlane_b32 s25, v0
	s_mul_i32 s24, s24, s25
	s_mul_hi_u32 s24, s25, s24
	s_add_i32 s25, s25, s24
	s_mul_hi_u32 s24, s21, s25
	s_mul_i32 s25, s24, s20
	s_sub_i32 s21, s21, s25
	s_add_i32 s25, s24, 1
	s_sub_i32 s28, s21, s20
	s_cmp_ge_u32 s21, s20
	s_cselect_b32 s24, s25, s24
	s_cselect_b32 s21, s28, s21
	s_add_i32 s25, s24, 1
	s_cmp_ge_u32 s21, s20
	s_cselect_b32 s20, s25, s24
	s_xor_b32 s20, s20, s5
	s_sub_i32 s58, s20, s5
	s_mul_i32 s5, s58, s7
	s_sub_i32 s4, s4, s5
	s_add_i32 s57, s4, s6
	s_ashr_i32 s4, s58, 31
	s_mul_i32 s4, s16, s4
	s_mul_hi_u32 s5, s16, s58
	s_add_i32 s6, s5, s4
	s_lshr_b64 s[4:5], s[18:19], 23
	s_mul_i32 s4, s4, s58
	s_add_i32 s6, s6, s4
	s_mul_i32 s4, s16, s58
	s_waitcnt lgkmcnt(0)
	s_add_u32 s24, s12, s4
	s_addc_u32 s25, s13, s6
	s_lshl_b32 s4, s57, 14
	s_ashr_i32 s5, s4, 31
	s_lshl_b64 s[4:5], s[4:5], 1
	s_add_u32 s4, s8, s4
	s_addc_u32 s5, s9, s5
	s_lshl_b32 s6, s57, 15
	v_mul_lo_u32 v4, s18, v182
	v_lshl_or_b32 v168, v3, 7, v176
	v_mul_lo_u32 v3, s18, v180
	s_ashr_i32 s7, s6, 31
	v_add_lshl_u32 v160, v4, v177, 1
	v_add_lshl_u32 v162, v3, v177, 1
	v_lshlrev_b32_e32 v171, 1, v2
	s_lshl_b64 s[6:7], s[6:7], 1
	s_add_u32 s6, s10, s6
	s_addc_u32 s7, s11, s7
	s_nop 4
	global_load_dwordx4 v[24:27], v168, s[4:5]
	global_load_dwordx4 v[28:31], v170, s[4:5]
	global_load_dwordx4 v[32:35], v169, s[6:7]
	s_add_i32 s34, s44, 0
	global_load_dwordx4 v[36:39], v171, s[6:7]
	s_add_i32 m0, s34, 0x10000
	v_add_u32_e32 v175, 0, v1
	global_load_lds_dwordx4 v160, s[24:25]
	s_add_i32 m0, s34, 0x12000
	s_add_u32 s20, s4, 0x4000
	s_addc_u32 s21, s5, 0
	global_load_lds_dwordx4 v162, s[24:25]
	s_add_u32 s28, s6, 0x8000
	s_addc_u32 s29, s7, 0
	s_nop 4
	global_load_dwordx4 v[40:43], v168, s[20:21]
	global_load_dwordx4 v[44:47], v170, s[20:21]
	global_load_dwordx4 v[48:51], v169, s[28:29]
	global_load_dwordx4 v[52:55], v171, s[28:29]
	s_add_u32 s20, s24, s14
	s_addc_u32 s21, s25, s15
	s_add_i32 m0, s34, 0x14000
	v_mov_b32_e32 v161, 0
	global_load_lds_dwordx4 v160, s[20:21]
	s_add_i32 m0, s34, 0x16000
	s_add_u32 s28, s4, 0x80
	s_addc_u32 s29, s5, 0
	global_load_lds_dwordx4 v162, s[20:21]
	s_add_u32 s30, s6, 0x80
	s_addc_u32 s31, s7, 0
	s_nop 4
	global_load_dwordx4 v[56:59], v168, s[28:29]
	v_mov_b32_e32 v163, v161
	global_load_dwordx4 v[60:63], v170, s[28:29]
	v_lshl_add_u64 v[18:19], s[24:25], 0, v[160:161]
	v_lshl_add_u64 v[16:17], s[20:21], 0, v[160:161]
	v_lshl_add_u64 v[22:23], s[20:21], 0, v[162:163]
	s_mov_b64 s[20:21], 0x80
	global_load_dwordx4 v[64:67], v169, s[30:31]
	v_lshl_add_u64 v[20:21], s[24:25], 0, v[162:163]
	global_load_dwordx4 v[68:71], v171, s[30:31]
	s_add_i32 m0, s34, 0x18000
	v_lshl_add_u64 v[18:19], v[18:19], 0, s[20:21]
	global_load_lds_dwordx4 v[18:19], off
	v_lshl_add_u64 v[18:19], v[20:21], 0, s[20:21]
	s_add_i32 m0, s34, 0x1a000
	s_add_u32 s4, s4, 0x4080
	s_addc_u32 s5, s5, 0
	global_load_lds_dwordx4 v[18:19], off
	s_add_u32 s6, s6, 0x8080
	s_addc_u32 s7, s7, 0
	s_nop 4
	global_load_dwordx4 v[8:11], v168, s[4:5]
	global_load_dwordx4 v[0:3], v170, s[4:5]
	global_load_dwordx4 v[12:15], v169, s[6:7]
	global_load_dwordx4 v[4:7], v171, s[6:7]
	s_add_i32 m0, s34, 0x1c000
	v_lshl_add_u64 v[16:17], v[16:17], 0, s[20:21]
	global_load_lds_dwordx4 v[16:17], off
	v_lshl_add_u64 v[16:17], v[22:23], 0, s[20:21]
	s_add_i32 m0, s34, 0x1e000
	s_nop 0
	global_load_lds_dwordx4 v[16:17], off
	s_waitcnt vmcnt(20)
	v_pk_add_f16 v24, v24, v32
	v_pk_add_f16 v25, v25, v33
	v_pk_add_f16 v26, v26, v34
	v_pk_add_f16 v27, v27, v35
	v_pk_max_f16 v24, v24, 0
	v_pk_max_f16 v25, v25, 0
	v_pk_max_f16 v26, v26, 0
	v_pk_max_f16 v27, v27, 0
	v_pk_add_f16 v28, v28, v36
	v_pk_add_f16 v29, v29, v37
	v_pk_add_f16 v30, v30, v38
	v_pk_add_f16 v31, v31, v39
	v_pk_max_f16 v28, v28, 0
	v_pk_max_f16 v29, v29, 0
	v_pk_max_f16 v30, v30, 0
	v_pk_max_f16 v31, v31, 0
	ds_write_b128 v175, v[24:27]
	ds_write_b128 v175, v[28:31] offset:8192
	s_waitcnt vmcnt(14)
	v_pk_add_f16 v40, v40, v48
	v_pk_add_f16 v41, v41, v49
	v_pk_add_f16 v42, v42, v50
	v_pk_add_f16 v43, v43, v51
	v_pk_max_f16 v40, v40, 0
	v_pk_max_f16 v41, v41, 0
	v_pk_max_f16 v42, v42, 0
	v_pk_max_f16 v43, v43, 0
	v_pk_add_f16 v44, v44, v52
	v_pk_add_f16 v45, v45, v53
	v_pk_add_f16 v46, v46, v54
	v_pk_add_f16 v47, v47, v55
	v_pk_max_f16 v44, v44, 0
	v_pk_max_f16 v45, v45, 0
	v_pk_max_f16 v46, v46, 0
	v_pk_max_f16 v47, v47, 0
	ds_write_b128 v175, v[40:43] offset:16384
	ds_write_b128 v175, v[44:47] offset:24576
	s_waitcnt vmcnt(8)
	v_pk_add_f16 v56, v56, v64
	v_pk_add_f16 v57, v57, v65
	v_pk_add_f16 v58, v58, v66
	v_pk_add_f16 v59, v59, v67
	v_pk_max_f16 v56, v56, 0
	v_pk_max_f16 v57, v57, 0
	v_pk_max_f16 v58, v58, 0
	v_pk_max_f16 v59, v59, 0
	v_pk_add_f16 v60, v60, v68
	v_pk_add_f16 v61, v61, v69
	v_pk_add_f16 v62, v62, v70
	v_pk_add_f16 v63, v63, v71
	v_pk_max_f16 v60, v60, 0
	v_pk_max_f16 v61, v61, 0
	v_pk_max_f16 v62, v62, 0
	v_pk_max_f16 v63, v63, 0
	ds_write_b128 v175, v[56:59] offset:32768
	ds_write_b128 v175, v[60:63] offset:40960
	s_cmp_lg_u32 s27, 1
	s_load_dwordx4 s[4:7], s[0:1], 0x68
	s_load_dword s47, s[0:1], 0x78
	s_mov_b32 s48, 0
	s_cbranch_scc1 .LBB8_32
	s_barrier
